# PEER select gates: 16-lane softmax denominator by DPP row reduction instead of ds_bpermute butterfly (on top of u-sweep barrier + hoisted offsets)
# baseline (speedup 1.0000x reference)
; __device__ __forceinline__ void peer_select_phase(const Args& a, int layer, LAS unsigned char* lds, int G, int bid) {
;     ...
;         const float cv = SV[ci] + SV[16 + cj];
;         const unsigned ck = lane < 50 ? ord_key(cv, (unsigned)(ci * 16 + cj), 255u) : 0u;
;         int rc = 0;
; #pragma unroll 2
;         for (int m = 0; m < 50; m += 5) rank5(rc, (unsigned)__builtin_amdgcn_readlane((int)ck, m), (unsigned)__builtin_amdgcn_readlane((int)ck, m + 1), (unsigned)__builtin_amdgcn_readlane((int)ck, m + 2),
;                                               (unsigned)__builtin_amdgcn_readlane((int)ck, m + 3), (unsigned)__builtin_amdgcn_readlane((int)ck, m + 4), ck);
;         if (lane < 50 && rc < 16) { SV[32 + rc] = cv; SI[32 + rc] = ci * 16 + cj; }
.LBB0_1115:
	s_lshl_b32 s100, s46, 1
	s_add_i32 s100, s100, 0xfffe1800
	v_mbcnt_lo_u32_b32 v164, -1, 0
	v_mbcnt_hi_u32_b32 v164, -1, v164
	v_lshl_add_u32 v164, v164, 2, s100
	ds_write_b32 v164, v138
	v_mov_b32_e32 v164, s100
	v_mov_b32_e32 v165, 0
	s_waitcnt lgkmcnt(0)
	ds_read_b128 v[168:171], v164
	ds_read_b128 v[172:175], v164 offset:16
	ds_read_b128 v[176:179], v164 offset:32
	ds_read_b128 v[180:183], v164 offset:48
	ds_read_b128 v[184:187], v164 offset:64
	ds_read_b128 v[188:191], v164 offset:80
	ds_read_b128 v[192:195], v164 offset:96
	ds_read_b128 v[196:199], v164 offset:112
	ds_read_b128 v[200:203], v164 offset:128
	ds_read_b128 v[204:207], v164 offset:144
	ds_read_b128 v[208:211], v164 offset:160
	ds_read_b128 v[212:215], v164 offset:176
	ds_read_b128 v[216:219], v164 offset:192
	s_waitcnt lgkmcnt(11)
	v_cmp_gt_u32_e64 s[80:81], v168, v138
	v_cmp_gt_u32_e64 s[82:83], v169, v138
	v_cmp_gt_u32_e64 s[84:85], v170, v138
	v_cmp_gt_u32_e64 s[86:87], v171, v138
	v_addc_co_u32_e64 v136, s[96:97], 0, v136, s[80:81]
	v_addc_co_u32_e64 v136, s[96:97], 0, v136, s[82:83]
	v_addc_co_u32_e64 v136, s[96:97], 0, v136, s[84:85]
	v_addc_co_u32_e64 v136, s[96:97], 0, v136, s[86:87]
	v_cmp_gt_u32_e64 s[80:81], v172, v138
	v_cmp_gt_u32_e64 s[82:83], v173, v138
	v_cmp_gt_u32_e64 s[84:85], v174, v138
	v_cmp_gt_u32_e64 s[86:87], v175, v138
	v_addc_co_u32_e64 v165, s[96:97], 0, v165, s[80:81]
	v_addc_co_u32_e64 v165, s[96:97], 0, v165, s[82:83]
	v_addc_co_u32_e64 v165, s[96:97], 0, v165, s[84:85]
	v_addc_co_u32_e64 v165, s[96:97], 0, v165, s[86:87]
	s_waitcnt lgkmcnt(9)
	v_cmp_gt_u32_e64 s[80:81], v176, v138
	v_cmp_gt_u32_e64 s[82:83], v177, v138
	v_cmp_gt_u32_e64 s[84:85], v178, v138
	v_cmp_gt_u32_e64 s[86:87], v179, v138
	v_addc_co_u32_e64 v136, s[96:97], 0, v136, s[80:81]
	v_addc_co_u32_e64 v136, s[96:97], 0, v136, s[82:83]
	v_addc_co_u32_e64 v136, s[96:97], 0, v136, s[84:85]
	v_addc_co_u32_e64 v136, s[96:97], 0, v136, s[86:87]
	v_cmp_gt_u32_e64 s[80:81], v180, v138
	v_cmp_gt_u32_e64 s[82:83], v181, v138
	v_cmp_gt_u32_e64 s[84:85], v182, v138
	v_cmp_gt_u32_e64 s[86:87], v183, v138
	v_addc_co_u32_e64 v165, s[96:97], 0, v165, s[80:81]
	v_addc_co_u32_e64 v165, s[96:97], 0, v165, s[82:83]
	v_addc_co_u32_e64 v165, s[96:97], 0, v165, s[84:85]
	v_addc_co_u32_e64 v165, s[96:97], 0, v165, s[86:87]
	s_waitcnt lgkmcnt(7)
	v_cmp_gt_u32_e64 s[80:81], v184, v138
	v_cmp_gt_u32_e64 s[82:83], v185, v138
	v_cmp_gt_u32_e64 s[84:85], v186, v138
	v_cmp_gt_u32_e64 s[86:87], v187, v138
	v_addc_co_u32_e64 v136, s[96:97], 0, v136, s[80:81]
	v_addc_co_u32_e64 v136, s[96:97], 0, v136, s[82:83]
	v_addc_co_u32_e64 v136, s[96:97], 0, v136, s[84:85]
	v_addc_co_u32_e64 v136, s[96:97], 0, v136, s[86:87]
	v_cmp_gt_u32_e64 s[80:81], v188, v138
	v_cmp_gt_u32_e64 s[82:83], v189, v138
	v_cmp_gt_u32_e64 s[84:85], v190, v138
	v_cmp_gt_u32_e64 s[86:87], v191, v138
	v_addc_co_u32_e64 v165, s[96:97], 0, v165, s[80:81]
	v_addc_co_u32_e64 v165, s[96:97], 0, v165, s[82:83]
	v_addc_co_u32_e64 v165, s[96:97], 0, v165, s[84:85]
	v_addc_co_u32_e64 v165, s[96:97], 0, v165, s[86:87]
	s_waitcnt lgkmcnt(5)
	v_cmp_gt_u32_e64 s[80:81], v192, v138
	v_cmp_gt_u32_e64 s[82:83], v193, v138
	v_cmp_gt_u32_e64 s[84:85], v194, v138
	v_cmp_gt_u32_e64 s[86:87], v195, v138
	v_addc_co_u32_e64 v136, s[96:97], 0, v136, s[80:81]
	v_addc_co_u32_e64 v136, s[96:97], 0, v136, s[82:83]
	v_addc_co_u32_e64 v136, s[96:97], 0, v136, s[84:85]
	v_addc_co_u32_e64 v136, s[96:97], 0, v136, s[86:87]
	v_cmp_gt_u32_e64 s[80:81], v196, v138
	v_cmp_gt_u32_e64 s[82:83], v197, v138
	v_cmp_gt_u32_e64 s[84:85], v198, v138
	v_cmp_gt_u32_e64 s[86:87], v199, v138
	v_addc_co_u32_e64 v165, s[96:97], 0, v165, s[80:81]
	v_addc_co_u32_e64 v165, s[96:97], 0, v165, s[82:83]
	v_addc_co_u32_e64 v165, s[96:97], 0, v165, s[84:85]
	v_addc_co_u32_e64 v165, s[96:97], 0, v165, s[86:87]
	s_waitcnt lgkmcnt(3)
	v_cmp_gt_u32_e64 s[80:81], v200, v138
	v_cmp_gt_u32_e64 s[82:83], v201, v138
	v_cmp_gt_u32_e64 s[84:85], v202, v138
	v_cmp_gt_u32_e64 s[86:87], v203, v138
	v_addc_co_u32_e64 v136, s[96:97], 0, v136, s[80:81]
	v_addc_co_u32_e64 v136, s[96:97], 0, v136, s[82:83]
	v_addc_co_u32_e64 v136, s[96:97], 0, v136, s[84:85]
	v_addc_co_u32_e64 v136, s[96:97], 0, v136, s[86:87]
	v_cmp_gt_u32_e64 s[80:81], v204, v138
	v_cmp_gt_u32_e64 s[82:83], v205, v138
	v_cmp_gt_u32_e64 s[84:85], v206, v138
	v_cmp_gt_u32_e64 s[86:87], v207, v138
	v_addc_co_u32_e64 v165, s[96:97], 0, v165, s[80:81]
	v_addc_co_u32_e64 v165, s[96:97], 0, v165, s[82:83]
	v_addc_co_u32_e64 v165, s[96:97], 0, v165, s[84:85]
	v_addc_co_u32_e64 v165, s[96:97], 0, v165, s[86:87]
	s_waitcnt lgkmcnt(1)
; #define LDS_WAIT() asm volatile("s_waitcnt lgkmcnt(0)" ::: "memory")
; __device__ __forceinline__ void peer_select_phase(const Args& a, int layer, LAS unsigned char* lds, int G, int bid) {
;     ...
;         if (lane < 50 && rc < 16) { SV[32 + rc] = cv; SI[32 + rc] = ci * 16 + cj; }
;         LDS_WAIT();
;         {
;             const int ll = lane & 15;
;             const float ts = SV[32 + ll]; const int tp = SI[32 + ll];
;             const int e1 = SI[(tp >> 4) & 15], e2 = SI[16 + (tp & 15)];
;             const float mx = SV[32];
;             const float ex = __expf(rstd_t * (ts - mx));
;             float sm = ex; sm += __shfl_xor(sm, 8); sm += __shfl_xor(sm, 4); sm += __shfl_xor(sm, 2); sm += __shfl_xor(sm, 1);
;             if (lane < 16) { IDX[(size_t)tok * 128 + hd * 16 + lane] = e1 * 128 + e2; GATE[(size_t)tok * 128 + hd * 16 + lane] = ex / sm; }
	v_cmp_gt_u32_e64 s[80:81], v208, v138
	v_cmp_gt_u32_e64 s[82:83], v209, v138
	v_cmp_gt_u32_e64 s[84:85], v210, v138
	v_cmp_gt_u32_e64 s[86:87], v211, v138
	v_addc_co_u32_e64 v136, s[96:97], 0, v136, s[80:81]
	v_addc_co_u32_e64 v136, s[96:97], 0, v136, s[82:83]
	v_addc_co_u32_e64 v136, s[96:97], 0, v136, s[84:85]
	v_addc_co_u32_e64 v136, s[96:97], 0, v136, s[86:87]
	v_cmp_gt_u32_e64 s[80:81], v212, v138
	v_cmp_gt_u32_e64 s[82:83], v213, v138
	v_cmp_gt_u32_e64 s[84:85], v214, v138
	v_cmp_gt_u32_e64 s[86:87], v215, v138
	v_addc_co_u32_e64 v165, s[96:97], 0, v165, s[80:81]
	v_addc_co_u32_e64 v165, s[96:97], 0, v165, s[82:83]
	v_addc_co_u32_e64 v165, s[96:97], 0, v165, s[84:85]
	v_addc_co_u32_e64 v165, s[96:97], 0, v165, s[86:87]
	s_waitcnt lgkmcnt(0)
	v_cmp_gt_u32_e64 s[80:81], v216, v138
	v_cmp_gt_u32_e64 s[82:83], v217, v138
	v_cmp_gt_u32_e64 s[84:85], v218, v138
	v_cmp_gt_u32_e64 s[86:87], v219, v138
	v_addc_co_u32_e64 v136, s[96:97], 0, v136, s[80:81]
	v_addc_co_u32_e64 v136, s[96:97], 0, v136, s[82:83]
	v_addc_co_u32_e64 v136, s[96:97], 0, v136, s[84:85]
	v_addc_co_u32_e64 v136, s[96:97], 0, v136, s[86:87]
	v_add_u32_e32 v136, v136, v165
	v_cmp_gt_i32_e32 vcc, 16, v136
	s_and_b64 s[12:13], s[6:7], vcc
	s_and_saveexec_b64 s[10:11], s[12:13]
	v_lshl_add_u32 v136, v136, 2, s46
	ds_write2_b32 v136, v131, v150 offset0:32 offset1:80
	s_or_b64 exec, exec, s[10:11]
	s_waitcnt lgkmcnt(0)
	v_mov_b32_e32 v131, s46
	ds_read_b32 v136, v151 offset:128
	ds_read_b32 v131, v131 offset:128
	v_and_b32_e32 v139, 64, v135
	v_xor_b32_e32 v138, 8, v135
	v_xor_b32_e32 v142, 2, v135
	v_xor_b32_e32 v143, 1, v135
	s_waitcnt lgkmcnt(0)
	v_sub_f32_e32 v131, v136, v131
	v_mul_f32_e32 v131, v156, v131
	v_mul_f32_e32 v131, 0x3fb8aa3b, v131
	v_exp_f32_e32 v141, v131
	v_add_u32_e32 v136, 64, v139
	v_cmp_lt_i32_e32 vcc, v138, v136
	v_xor_b32_e32 v139, 4, v135
	s_nop 0
	v_cndmask_b32_e32 v131, v135, v138, vcc
	v_lshlrev_b32_e32 v131, 2, v131
	v_add_f32_dpp v164, v141, v141 quad_perm:[1,0,3,2] row_mask:0xf bank_mask:0xf bound_ctrl:1
	v_cmp_lt_i32_e32 vcc, v139, v136
	s_nop 1
	v_cndmask_b32_e32 v139, v135, v139, vcc
	v_add_f32_dpp v164, v164, v164 quad_perm:[2,3,0,1] row_mask:0xf bank_mask:0xf bound_ctrl:1
	v_lshlrev_b32_e32 v138, 2, v139
	v_cmp_lt_i32_e32 vcc, v142, v136
	s_nop 1
	v_cndmask_b32_e32 v142, v135, v142, vcc
	v_add_f32_dpp v164, v164, v164 row_ror:4 row_mask:0xf bank_mask:0xf bound_ctrl:1
	v_lshlrev_b32_e32 v139, 2, v142
	v_cmp_lt_i32_e32 vcc, v143, v136
	s_nop 1
	v_cndmask_b32_e32 v143, v135, v143, vcc
	v_add_f32_dpp v142, v164, v164 row_ror:8 row_mask:0xf bank_mask:0xf bound_ctrl:1
	v_lshlrev_b32_e32 v140, 2, v143
	v_mov_b32_e32 v143, 0
	s_and_saveexec_b64 s[10:11], s[8:9]
	s_cbranch_execz .LBB0_1120
	ds_read_b32 v144, v151 offset:320
	s_waitcnt lgkmcnt(1)
	v_add_f32_e32 v156, v142, v143
	s_ashr_i32 s12, s58, 3
	v_div_scale_f32 v158, s[30:31], v156, v156, v141
	s_waitcnt lgkmcnt(0)
	v_and_b32_e32 v145, 15, v144
	v_lshrrev_b32_e32 v144, 2, v144
	v_and_b32_e32 v144, 60, v144
	v_lshl_add_u32 v145, v145, 2, s46
	v_add_u32_e32 v144, s46, v144
	ds_read_b32 v145, v145 offset:256
	ds_read_b32 v144, v144 offset:192
	s_ashr_i32 s13, s12, 31
	v_rcp_f32_e32 v159, v158
	s_lshl_b64 s[12:13], s[12:13], 9
	v_lshl_or_b32 v142, v134, 2, s12
	v_mov_b32_e32 v143, s13
	s_waitcnt lgkmcnt(0)
	v_lshl_add_u32 v157, v144, 7, v145
	v_lshl_add_u64 v[144:145], s[18:19], 0, v[142:143]
	global_store_dword v[144:145], v157, off
	v_fma_f32 v144, -v158, v159, 1.0
	v_fmac_f32_e32 v159, v144, v159
	v_div_scale_f32 v144, vcc, v141, v156, v141
	v_mul_f32_e32 v145, v144, v159
	v_fma_f32 v157, -v158, v145, v144
	v_fmac_f32_e32 v145, v157, v159
	v_fma_f32 v144, -v158, v145, v144
	v_div_fmas_f32 v144, v144, v159, v145
	v_div_fixup_f32 v141, v144, v156, v141
	v_lshl_add_u64 v[142:143], s[20:21], 0, v[142:143]
	global_store_dword v[142:143], v141, off

; __device__ __forceinline__ void peer_select_phase(const Args& a, int layer, LAS unsigned char* lds, int G, int bid) {
;     ...
;         const float cv = SV[ci] + SV[16 + cj];
;         const unsigned ck = lane < 50 ? ord_key(cv, (unsigned)(ci * 16 + cj), 255u) : 0u;
;         int rc = 0;
; #pragma unroll 2
;         for (int m = 0; m < 50; m += 5) rank5(rc, (unsigned)__builtin_amdgcn_readlane((int)ck, m), (unsigned)__builtin_amdgcn_readlane((int)ck, m + 1), (unsigned)__builtin_amdgcn_readlane((int)ck, m + 2),
;                                               (unsigned)__builtin_amdgcn_readlane((int)ck, m + 3), (unsigned)__builtin_amdgcn_readlane((int)ck, m + 4), ck);
;         if (lane < 50 && rc < 16) { SV[32 + rc] = cv; SI[32 + rc] = ci * 16 + cj; }
.LBB0_2176:
	s_lshl_b32 s100, s50, 1
	s_add_i32 s100, s100, 0xfffe1800
	v_mbcnt_lo_u32_b32 v164, -1, 0
	v_mbcnt_hi_u32_b32 v164, -1, v164
	v_lshl_add_u32 v164, v164, 2, s100
	ds_write_b32 v164, v138
	v_mov_b32_e32 v164, s100
	v_mov_b32_e32 v165, 0
	s_waitcnt lgkmcnt(0)
	ds_read_b128 v[168:171], v164
	ds_read_b128 v[172:175], v164 offset:16
	ds_read_b128 v[176:179], v164 offset:32
	ds_read_b128 v[180:183], v164 offset:48
	ds_read_b128 v[184:187], v164 offset:64
	ds_read_b128 v[188:191], v164 offset:80
	ds_read_b128 v[192:195], v164 offset:96
	ds_read_b128 v[196:199], v164 offset:112
	ds_read_b128 v[200:203], v164 offset:128
	ds_read_b128 v[204:207], v164 offset:144
	ds_read_b128 v[208:211], v164 offset:160
	ds_read_b128 v[212:215], v164 offset:176
	ds_read_b128 v[216:219], v164 offset:192
	s_waitcnt lgkmcnt(11)
	v_cmp_gt_u32_e64 s[80:81], v168, v138
	v_cmp_gt_u32_e64 s[82:83], v169, v138
	v_cmp_gt_u32_e64 s[84:85], v170, v138
	v_cmp_gt_u32_e64 s[86:87], v171, v138
	v_addc_co_u32_e64 v136, s[96:97], 0, v136, s[80:81]
	v_addc_co_u32_e64 v136, s[96:97], 0, v136, s[82:83]
	v_addc_co_u32_e64 v136, s[96:97], 0, v136, s[84:85]
	v_addc_co_u32_e64 v136, s[96:97], 0, v136, s[86:87]
	v_cmp_gt_u32_e64 s[80:81], v172, v138
	v_cmp_gt_u32_e64 s[82:83], v173, v138
	v_cmp_gt_u32_e64 s[84:85], v174, v138
	v_cmp_gt_u32_e64 s[86:87], v175, v138
	v_addc_co_u32_e64 v165, s[96:97], 0, v165, s[80:81]
	v_addc_co_u32_e64 v165, s[96:97], 0, v165, s[82:83]
	v_addc_co_u32_e64 v165, s[96:97], 0, v165, s[84:85]
	v_addc_co_u32_e64 v165, s[96:97], 0, v165, s[86:87]
	s_waitcnt lgkmcnt(9)
	v_cmp_gt_u32_e64 s[80:81], v176, v138
	v_cmp_gt_u32_e64 s[82:83], v177, v138
	v_cmp_gt_u32_e64 s[84:85], v178, v138
	v_cmp_gt_u32_e64 s[86:87], v179, v138
	v_addc_co_u32_e64 v136, s[96:97], 0, v136, s[80:81]
	v_addc_co_u32_e64 v136, s[96:97], 0, v136, s[82:83]
	v_addc_co_u32_e64 v136, s[96:97], 0, v136, s[84:85]
	v_addc_co_u32_e64 v136, s[96:97], 0, v136, s[86:87]
	v_cmp_gt_u32_e64 s[80:81], v180, v138
	v_cmp_gt_u32_e64 s[82:83], v181, v138
	v_cmp_gt_u32_e64 s[84:85], v182, v138
	v_cmp_gt_u32_e64 s[86:87], v183, v138
	v_addc_co_u32_e64 v165, s[96:97], 0, v165, s[80:81]
	v_addc_co_u32_e64 v165, s[96:97], 0, v165, s[82:83]
	v_addc_co_u32_e64 v165, s[96:97], 0, v165, s[84:85]
	v_addc_co_u32_e64 v165, s[96:97], 0, v165, s[86:87]
	s_waitcnt lgkmcnt(7)
	v_cmp_gt_u32_e64 s[80:81], v184, v138
	v_cmp_gt_u32_e64 s[82:83], v185, v138
	v_cmp_gt_u32_e64 s[84:85], v186, v138
	v_cmp_gt_u32_e64 s[86:87], v187, v138
	v_addc_co_u32_e64 v136, s[96:97], 0, v136, s[80:81]
	v_addc_co_u32_e64 v136, s[96:97], 0, v136, s[82:83]
	v_addc_co_u32_e64 v136, s[96:97], 0, v136, s[84:85]
	v_addc_co_u32_e64 v136, s[96:97], 0, v136, s[86:87]
	v_cmp_gt_u32_e64 s[80:81], v188, v138
	v_cmp_gt_u32_e64 s[82:83], v189, v138
	v_cmp_gt_u32_e64 s[84:85], v190, v138
	v_cmp_gt_u32_e64 s[86:87], v191, v138
	v_addc_co_u32_e64 v165, s[96:97], 0, v165, s[80:81]
	v_addc_co_u32_e64 v165, s[96:97], 0, v165, s[82:83]
	v_addc_co_u32_e64 v165, s[96:97], 0, v165, s[84:85]
	v_addc_co_u32_e64 v165, s[96:97], 0, v165, s[86:87]
	s_waitcnt lgkmcnt(5)
	v_cmp_gt_u32_e64 s[80:81], v192, v138
	v_cmp_gt_u32_e64 s[82:83], v193, v138
	v_cmp_gt_u32_e64 s[84:85], v194, v138
	v_cmp_gt_u32_e64 s[86:87], v195, v138
	v_addc_co_u32_e64 v136, s[96:97], 0, v136, s[80:81]
	v_addc_co_u32_e64 v136, s[96:97], 0, v136, s[82:83]
	v_addc_co_u32_e64 v136, s[96:97], 0, v136, s[84:85]
	v_addc_co_u32_e64 v136, s[96:97], 0, v136, s[86:87]
	v_cmp_gt_u32_e64 s[80:81], v196, v138
	v_cmp_gt_u32_e64 s[82:83], v197, v138
	v_cmp_gt_u32_e64 s[84:85], v198, v138
	v_cmp_gt_u32_e64 s[86:87], v199, v138
	v_addc_co_u32_e64 v165, s[96:97], 0, v165, s[80:81]
	v_addc_co_u32_e64 v165, s[96:97], 0, v165, s[82:83]
	v_addc_co_u32_e64 v165, s[96:97], 0, v165, s[84:85]
	v_addc_co_u32_e64 v165, s[96:97], 0, v165, s[86:87]
	s_waitcnt lgkmcnt(3)
	v_cmp_gt_u32_e64 s[80:81], v200, v138
	v_cmp_gt_u32_e64 s[82:83], v201, v138
	v_cmp_gt_u32_e64 s[84:85], v202, v138
	v_cmp_gt_u32_e64 s[86:87], v203, v138
	v_addc_co_u32_e64 v136, s[96:97], 0, v136, s[80:81]
	v_addc_co_u32_e64 v136, s[96:97], 0, v136, s[82:83]
	v_addc_co_u32_e64 v136, s[96:97], 0, v136, s[84:85]
	v_addc_co_u32_e64 v136, s[96:97], 0, v136, s[86:87]
	v_cmp_gt_u32_e64 s[80:81], v204, v138
	v_cmp_gt_u32_e64 s[82:83], v205, v138
	v_cmp_gt_u32_e64 s[84:85], v206, v138
	v_cmp_gt_u32_e64 s[86:87], v207, v138
	v_addc_co_u32_e64 v165, s[96:97], 0, v165, s[80:81]
	v_addc_co_u32_e64 v165, s[96:97], 0, v165, s[82:83]
	v_addc_co_u32_e64 v165, s[96:97], 0, v165, s[84:85]
	v_addc_co_u32_e64 v165, s[96:97], 0, v165, s[86:87]
	s_waitcnt lgkmcnt(1)
; #define LDS_WAIT() asm volatile("s_waitcnt lgkmcnt(0)" ::: "memory")
; __device__ __forceinline__ void peer_select_phase(const Args& a, int layer, LAS unsigned char* lds, int G, int bid) {
;     ...
;         if (lane < 50 && rc < 16) { SV[32 + rc] = cv; SI[32 + rc] = ci * 16 + cj; }
;         LDS_WAIT();
;         {
;             const int ll = lane & 15;
;             const float ts = SV[32 + ll]; const int tp = SI[32 + ll];
;             const int e1 = SI[(tp >> 4) & 15], e2 = SI[16 + (tp & 15)];
;             const float mx = SV[32];
;             const float ex = __expf(rstd_t * (ts - mx));
;             float sm = ex; sm += __shfl_xor(sm, 8); sm += __shfl_xor(sm, 4); sm += __shfl_xor(sm, 2); sm += __shfl_xor(sm, 1);
;             if (lane < 16) { IDX[(size_t)tok * 128 + hd * 16 + lane] = e1 * 128 + e2; GATE[(size_t)tok * 128 + hd * 16 + lane] = ex / sm; }
	v_cmp_gt_u32_e64 s[80:81], v208, v138
	v_cmp_gt_u32_e64 s[82:83], v209, v138
	v_cmp_gt_u32_e64 s[84:85], v210, v138
	v_cmp_gt_u32_e64 s[86:87], v211, v138
	v_addc_co_u32_e64 v136, s[96:97], 0, v136, s[80:81]
	v_addc_co_u32_e64 v136, s[96:97], 0, v136, s[82:83]
	v_addc_co_u32_e64 v136, s[96:97], 0, v136, s[84:85]
	v_addc_co_u32_e64 v136, s[96:97], 0, v136, s[86:87]
	v_cmp_gt_u32_e64 s[80:81], v212, v138
	v_cmp_gt_u32_e64 s[82:83], v213, v138
	v_cmp_gt_u32_e64 s[84:85], v214, v138
	v_cmp_gt_u32_e64 s[86:87], v215, v138
	v_addc_co_u32_e64 v165, s[96:97], 0, v165, s[80:81]
	v_addc_co_u32_e64 v165, s[96:97], 0, v165, s[82:83]
	v_addc_co_u32_e64 v165, s[96:97], 0, v165, s[84:85]
	v_addc_co_u32_e64 v165, s[96:97], 0, v165, s[86:87]
	s_waitcnt lgkmcnt(0)
	v_cmp_gt_u32_e64 s[80:81], v216, v138
	v_cmp_gt_u32_e64 s[82:83], v217, v138
	v_cmp_gt_u32_e64 s[84:85], v218, v138
	v_cmp_gt_u32_e64 s[86:87], v219, v138
	v_addc_co_u32_e64 v136, s[96:97], 0, v136, s[80:81]
	v_addc_co_u32_e64 v136, s[96:97], 0, v136, s[82:83]
	v_addc_co_u32_e64 v136, s[96:97], 0, v136, s[84:85]
	v_addc_co_u32_e64 v136, s[96:97], 0, v136, s[86:87]
	v_add_u32_e32 v136, v136, v165
	v_cmp_gt_i32_e32 vcc, 16, v136
	s_and_b64 s[12:13], s[6:7], vcc
	s_and_saveexec_b64 s[10:11], s[12:13]
	v_lshl_add_u32 v136, v136, 2, s50
	ds_write2_b32 v136, v131, v150 offset0:32 offset1:80
	s_or_b64 exec, exec, s[10:11]
	s_waitcnt lgkmcnt(0)
	v_mov_b32_e32 v131, s50
	ds_read_b32 v136, v151 offset:128
	ds_read_b32 v131, v131 offset:128
	v_and_b32_e32 v139, 64, v135
	v_xor_b32_e32 v138, 8, v135
	v_xor_b32_e32 v142, 2, v135
	v_xor_b32_e32 v143, 1, v135
	s_waitcnt lgkmcnt(0)
	v_sub_f32_e32 v131, v136, v131
	v_mul_f32_e32 v131, v156, v131
	v_mul_f32_e32 v131, 0x3fb8aa3b, v131
	v_exp_f32_e32 v141, v131
	v_add_u32_e32 v136, 64, v139
	v_cmp_lt_i32_e32 vcc, v138, v136
	v_xor_b32_e32 v139, 4, v135
	s_nop 0
	v_cndmask_b32_e32 v131, v135, v138, vcc
	v_lshlrev_b32_e32 v131, 2, v131
	v_add_f32_dpp v164, v141, v141 quad_perm:[1,0,3,2] row_mask:0xf bank_mask:0xf bound_ctrl:1
	v_cmp_lt_i32_e32 vcc, v139, v136
	s_nop 1
	v_cndmask_b32_e32 v139, v135, v139, vcc
	v_add_f32_dpp v164, v164, v164 quad_perm:[2,3,0,1] row_mask:0xf bank_mask:0xf bound_ctrl:1
	v_lshlrev_b32_e32 v138, 2, v139
	v_cmp_lt_i32_e32 vcc, v142, v136
	s_nop 1
	v_cndmask_b32_e32 v142, v135, v142, vcc
	v_add_f32_dpp v164, v164, v164 row_ror:4 row_mask:0xf bank_mask:0xf bound_ctrl:1
	v_lshlrev_b32_e32 v139, 2, v142
	v_cmp_lt_i32_e32 vcc, v143, v136
	s_nop 1
	v_cndmask_b32_e32 v143, v135, v143, vcc
	v_add_f32_dpp v142, v164, v164 row_ror:8 row_mask:0xf bank_mask:0xf bound_ctrl:1
	v_lshlrev_b32_e32 v140, 2, v143
	v_mov_b32_e32 v143, 0
	s_and_saveexec_b64 s[10:11], s[8:9]
	s_cbranch_execz .LBB0_2181
	ds_read_b32 v144, v151 offset:320
	s_waitcnt lgkmcnt(1)
	v_add_f32_e32 v156, v142, v143
	s_ashr_i32 s12, s62, 3
	v_div_scale_f32 v158, s[34:35], v156, v156, v141
	s_waitcnt lgkmcnt(0)
	v_and_b32_e32 v145, 15, v144
	v_lshrrev_b32_e32 v144, 2, v144
	v_and_b32_e32 v144, 60, v144
	v_lshl_add_u32 v145, v145, 2, s50
	v_add_u32_e32 v144, s50, v144
	ds_read_b32 v145, v145 offset:256
	ds_read_b32 v144, v144 offset:192
	s_ashr_i32 s13, s12, 31
	v_rcp_f32_e32 v159, v158
	s_lshl_b64 s[12:13], s[12:13], 9
	v_lshl_or_b32 v142, v134, 2, s12
	v_mov_b32_e32 v143, s13
	s_waitcnt lgkmcnt(0)
	v_lshl_add_u32 v157, v144, 7, v145
	v_lshl_add_u64 v[144:145], s[20:21], 0, v[142:143]
	global_store_dword v[144:145], v157, off
	v_fma_f32 v144, -v158, v159, 1.0
	v_fmac_f32_e32 v159, v144, v159
	v_div_scale_f32 v144, vcc, v141, v156, v141
	v_mul_f32_e32 v145, v144, v159
	v_fma_f32 v157, -v158, v145, v144
	v_fmac_f32_e32 v145, v157, v159
	v_fma_f32 v144, -v158, v145, v144
	v_div_fmas_f32 v144, v144, v159, v145
	v_div_fixup_f32 v141, v144, v156, v141
	v_lshl_add_u64 v[142:143], s[22:23], 0, v[142:143]
	global_store_dword v[142:143], v141, off
